# speedup vs baseline: 1.0715x; 1.0005x over previous
.Lagg_gmaxret_1:
	s_mov_b64 exec, s[66:67]
	v_fma_mix_f32 v32, v48, v42, 0 op_sel_hi:[1,0,0]
	v_fma_mix_f32 v33, v48, v42, 0 op_sel:[1,0,0] op_sel_hi:[1,0,0]
	v_fma_mix_f32 v34, v49, v42, 0 op_sel_hi:[1,0,0]
	v_fma_mix_f32 v35, v49, v42, 0 op_sel:[1,0,0] op_sel_hi:[1,0,0]
	v_fma_mix_f32 v36, v50, v42, 0 op_sel_hi:[1,0,0]
	v_fma_mix_f32 v37, v50, v42, 0 op_sel:[1,0,0] op_sel_hi:[1,0,0]
	v_fma_mix_f32 v38, v51, v42, 0 op_sel_hi:[1,0,0]
	v_fma_mix_f32 v39, v51, v42, 0 op_sel:[1,0,0] op_sel_hi:[1,0,0]
	v_fma_mix_f32 v56, v52, v42, 0 op_sel_hi:[1,0,0]
	v_fma_mix_f32 v57, v52, v42, 0 op_sel:[1,0,0] op_sel_hi:[1,0,0]
	v_fma_mix_f32 v58, v53, v42, 0 op_sel_hi:[1,0,0]
	v_fma_mix_f32 v59, v53, v42, 0 op_sel:[1,0,0] op_sel_hi:[1,0,0]
	v_fma_mix_f32 v60, v54, v42, 0 op_sel_hi:[1,0,0]
	v_fma_mix_f32 v61, v54, v42, 0 op_sel:[1,0,0] op_sel_hi:[1,0,0]
	v_fma_mix_f32 v62, v55, v42, 0 op_sel_hi:[1,0,0]
	v_fma_mix_f32 v63, v55, v42, 0 op_sel:[1,0,0] op_sel_hi:[1,0,0]
	v_fma_mix_f32 v32, v5, v15, v32 op_sel_hi:[1,0,0]
	v_fma_mix_f32 v33, v5, v15, v33 op_sel:[1,0,0] op_sel_hi:[1,0,0]
	v_fma_mix_f32 v34, v6, v15, v34 op_sel_hi:[1,0,0]
	v_fma_mix_f32 v35, v6, v15, v35 op_sel:[1,0,0] op_sel_hi:[1,0,0]
	v_fma_mix_f32 v36, v7, v15, v36 op_sel_hi:[1,0,0]
	v_fma_mix_f32 v37, v7, v15, v37 op_sel:[1,0,0] op_sel_hi:[1,0,0]
	v_fma_mix_f32 v38, v8, v15, v38 op_sel_hi:[1,0,0]
	v_fma_mix_f32 v39, v8, v15, v39 op_sel:[1,0,0] op_sel_hi:[1,0,0]
	v_fma_mix_f32 v56, v9, v15, v56 op_sel_hi:[1,0,0]
	v_fma_mix_f32 v57, v9, v15, v57 op_sel:[1,0,0] op_sel_hi:[1,0,0]
	v_fma_mix_f32 v58, v10, v15, v58 op_sel_hi:[1,0,0]
	v_fma_mix_f32 v59, v10, v15, v59 op_sel:[1,0,0] op_sel_hi:[1,0,0]
	v_fma_mix_f32 v60, v11, v15, v60 op_sel_hi:[1,0,0]
	v_fma_mix_f32 v61, v11, v15, v61 op_sel:[1,0,0] op_sel_hi:[1,0,0]
	v_fma_mix_f32 v62, v12, v15, v62 op_sel_hi:[1,0,0]
	v_fma_mix_f32 v63, v12, v15, v63 op_sel:[1,0,0] op_sel_hi:[1,0,0]
	s_waitcnt vmcnt(0)
	v_fma_mix_f32 v32, v24, v15, v32 op_sel_hi:[1,0,0]
	v_fma_mix_f32 v33, v24, v15, v33 op_sel:[1,0,0] op_sel_hi:[1,0,0]
	v_fma_mix_f32 v34, v25, v15, v34 op_sel_hi:[1,0,0]
	v_fma_mix_f32 v35, v25, v15, v35 op_sel:[1,0,0] op_sel_hi:[1,0,0]
	v_fma_mix_f32 v36, v26, v15, v36 op_sel_hi:[1,0,0]
	v_fma_mix_f32 v37, v26, v15, v37 op_sel:[1,0,0] op_sel_hi:[1,0,0]
	v_fma_mix_f32 v38, v27, v15, v38 op_sel_hi:[1,0,0]
	v_fma_mix_f32 v39, v27, v15, v39 op_sel:[1,0,0] op_sel_hi:[1,0,0]
	v_fma_mix_f32 v56, v28, v15, v56 op_sel_hi:[1,0,0]
	v_fma_mix_f32 v57, v28, v15, v57 op_sel:[1,0,0] op_sel_hi:[1,0,0]
	v_fma_mix_f32 v58, v29, v15, v58 op_sel_hi:[1,0,0]
	v_fma_mix_f32 v59, v29, v15, v59 op_sel:[1,0,0] op_sel_hi:[1,0,0]
	v_fma_mix_f32 v60, v30, v15, v60 op_sel_hi:[1,0,0]
	v_fma_mix_f32 v61, v30, v15, v61 op_sel:[1,0,0] op_sel_hi:[1,0,0]
	v_fma_mix_f32 v62, v31, v15, v62 op_sel_hi:[1,0,0]
	v_fma_mix_f32 v63, v31, v15, v63 op_sel:[1,0,0] op_sel_hi:[1,0,0]
	v_max_f32_e32 v32, 0, v32
	v_max_f32_e32 v33, 0, v33
	v_max_f32_e32 v34, 0, v34
	v_max_f32_e32 v35, 0, v35
	v_max_f32_e32 v36, 0, v36
	v_max_f32_e32 v37, 0, v37
	v_max_f32_e32 v38, 0, v38
	v_max_f32_e32 v39, 0, v39
	v_max_f32_e32 v56, 0, v56
	v_max_f32_e32 v57, 0, v57
	v_max_f32_e32 v58, 0, v58
	v_max_f32_e32 v59, 0, v59
	v_max_f32_e32 v60, 0, v60
	v_max_f32_e32 v61, 0, v61
	v_max_f32_e32 v62, 0, v62
	v_max_f32_e32 v63, 0, v63
	v_lshlrev_b32_e32 v40, 2, v0
	v_add_u32_e32 v44, 0x6200, v40
	ds_write_b32 v40, v32 offset:24448
	ds_write_b32 v40, v33 offset:27584
	ds_write_b32 v40, v34 offset:30720
	ds_write_b32 v40, v35 offset:33856
	ds_write_b32 v40, v36 offset:36992
	ds_write_b32 v40, v37 offset:40128
	ds_write_b32 v40, v38 offset:43264
	ds_write_b32 v40, v39 offset:46400
	ds_write_b32 v44, v56 offset:24448
	ds_write_b32 v44, v57 offset:27584
	ds_write_b32 v44, v58 offset:30720
	ds_write_b32 v44, v59 offset:33856
	ds_write_b32 v44, v60 offset:36992
	ds_write_b32 v44, v61 offset:40128
	ds_write_b32 v44, v62 offset:43264
	ds_write_b32 v44, v63 offset:46400
	v_lshrrev_b32_e32 v42, 4, v1
	v_mul_u32_u24_e32 v42, 0x3100, v42
	v_and_b32_e32 v43, -4, v0
	v_lshl_add_u32 v42, v43, 2, v42
	ds_read_b32 v32, v42 offset:24448
	ds_read_b32 v33, v42 offset:27584
	ds_read_b32 v34, v42 offset:30720
	ds_read_b32 v35, v42 offset:33856
	ds_read_b32 v36, v42 offset:24452
	ds_read_b32 v37, v42 offset:27588
	ds_read_b32 v38, v42 offset:30724
	ds_read_b32 v39, v42 offset:33860
	ds_read_b32 v56, v42 offset:24456
	ds_read_b32 v57, v42 offset:27592
	ds_read_b32 v58, v42 offset:30728
	ds_read_b32 v59, v42 offset:33864
	ds_read_b32 v60, v42 offset:24460
	ds_read_b32 v61, v42 offset:27596
	ds_read_b32 v62, v42 offset:30732
	ds_read_b32 v63, v42 offset:33868
	s_waitcnt lgkmcnt(12)
	global_store_dwordx4 v41, v[32:35], s[68:69] nt
	s_waitcnt lgkmcnt(8)
	global_store_dwordx4 v41, v[36:39], s[68:69] offset:64 nt
	s_waitcnt lgkmcnt(4)
	global_store_dwordx4 v41, v[56:59], s[68:69] offset:128 nt
	s_waitcnt lgkmcnt(0)
	global_store_dwordx4 v41, v[60:63], s[68:69] offset:192 nt
	s_nop 1
